# pipelined attention, weight-paced softmax VALU + barrier 3 fragments early
# speedup vs baseline: 1.0125x; 1.0007x over previous
.LBB0_733:
	s_or_b64 exec, exec, s[8:9]
	s_movk_i32 s4, 0xf0
	s_cmp_lg_u32 0, -1
	v_lshlrev_b32_e32 v39, 8, v141
	v_bitop3_b32 v80, v142, s4, v136 bitop3:0x48
	s_cselect_b32 s10, 0, 0
	v_cvt_pk_bf16_f32 v96, v134, v135
	v_cvt_pk_bf16_f32 v97, v132, v133
	v_cvt_pk_bf16_f32 v98, v130, v131
	v_cvt_pk_bf16_f32 v99, v128, v129
	v_cvt_pk_bf16_f32 v100, v126, v127
	v_cvt_pk_bf16_f32 v101, v124, v125
	v_cvt_pk_bf16_f32 v102, v122, v123
	v_cvt_pk_bf16_f32 v103, v120, v121
	v_cvt_pk_bf16_f32 v104, v70, v71
	v_cvt_pk_bf16_f32 v105, v74, v75
	v_cvt_pk_bf16_f32 v106, v64, v65
	v_cvt_pk_bf16_f32 v107, v68, v69
	v_cvt_pk_bf16_f32 v108, v60, v61
	v_cvt_pk_bf16_f32 v109, v66, v67
	v_cvt_pk_bf16_f32 v110, v56, v57
	v_cvt_pk_bf16_f32 v111, v58, v59
	v_cvt_pk_bf16_f32 v112, v112, v113
	v_cvt_pk_bf16_f32 v113, v118, v119
	v_cvt_pk_bf16_f32 v114, v114, v115
	v_cvt_pk_bf16_f32 v115, v116, v117
	v_cvt_pk_bf16_f32 v116, v78, v79
	v_cvt_pk_bf16_f32 v117, v76, v77
	v_cvt_pk_bf16_f32 v118, v72, v73
	v_cvt_pk_bf16_f32 v119, v62, v63
	v_cvt_pk_bf16_f32 v120, v52, v53
	v_cvt_pk_bf16_f32 v121, v54, v55
	v_cvt_pk_bf16_f32 v122, v46, v47
	v_cvt_pk_bf16_f32 v123, v50, v51
	v_cvt_pk_bf16_f32 v124, v44, v45
	v_cvt_pk_bf16_f32 v125, v48, v49
	v_cvt_pk_bf16_f32 v126, v40, v41
	v_cvt_pk_bf16_f32 v127, v42, v43
	v_readlane_b32 s100, v250, 8
	v_mbcnt_lo_u32_b32 v68, -1, 0
	v_mbcnt_hi_u32_b32 v68, -1, v68
	s_nop 1
	v_add_u32_e32 v69, s100, v68
	v_lshrrev_b32_e32 v70, 3, v69
	v_and_b32_e32 v71, 7, v69
	v_lshrrev_b32_e32 v72, 2, v71
	v_bfe_u32 v73, v71, 1, 1
	v_and_b32_e32 v74, 1, v71
	v_lshlrev_b32_e32 v74, 1, v74
	v_lshl_add_u32 v75, v72, 2, v74
	v_bfe_u32 v76, v70, 1, 3
	v_xor_b32_e32 v77, v75, v76
	v_add_u32_e32 v78, 1, v75
	v_xor_b32_e32 v78, v78, v76
	v_lshlrev_b32_e32 v79, 7, v70
	v_lshl_add_u32 v79, v73, 3, v79
	v_lshl_add_u32 v64, v77, 4, v79
	v_lshl_add_u32 v65, v78, 4, v79
	v_add_u32_e32 v66, 0x2000, v64
	v_add_u32_e32 v67, 0x2000, v65
	v_or_b32_e32 v81, v39, v80
	s_add_i32 s15, s10, 0x10000
	v_and_b32_e32 v82, 6, v137
	v_lshrrev_b32_e32 v84, 4, v136
	s_waitcnt vmcnt(0)
	s_waitcnt vmcnt(0)
	s_add_i32 s11, s10, 0x12000
	v_lshl_add_u32 v83, v139, 7, s10
	v_bitop3_b32 v85, v84, v82, 7 bitop3:0x6c
	v_and_b32_e32 v86, 8, v138
	v_or_b32_e32 v82, 1, v82
	v_add_u32_e32 v225, s15, v81
	s_waitcnt vmcnt(4)
	ds_write_b128 v225, v[24:27] offset:0
	v_lshlrev_b32_e32 v85, 4, v85
	v_add_u32_e32 v87, v83, v86
	v_bitop3_b32 v82, v84, v82, 7 bitop3:0x6c
	v_add3_u32 v226, v80, s11, v39
	ds_write_b128 v226, v[28:31] offset:0
	v_lshlrev_b32_e32 v82, 4, v82
	v_add_u32_e32 v227, v87, v85
	ds_write_b64 v64, v[12:13] offset:0
	v_lshrrev_b32_e32 v32, 5, v136
	v_add_u32_e32 v83, 0x2000, v83
	v_or_b32_e32 v84, v85, v86
	v_add_u32_e32 v228, v87, v82
	ds_write_b64 v65, v[14:15] offset:0
	v_xor_b32_e32 v32, v32, v137
	v_or_b32_e32 v86, v82, v86
	v_add_u32_e32 v229, v84, v83
	ds_write_b64 v66, v[4:5] offset:0
	v_lshlrev_b32_e32 v32, 4, v32
	v_add_u32_e32 v184, v86, v83
	ds_write_b64 v67, v[6:7] offset:0
	v_lshlrev_b32_e32 v33, 8, v143
	v_and_b32_e32 v32, 16, v32
	v_bfe_u32 v35, v137, 1, 3
	s_waitcnt vmcnt(4)
	ds_write_b128 v225, v[20:23] offset:0x4000
	v_lshlrev_b32_e32 v36, 5, v35
	v_add3_u32 v32, v33, s15, v32
	s_movk_i32 s16, 0x60
	ds_write_b128 v226, v[16:19] offset:0x4000
	v_xad_u32 v204, v36, s16, v32
	s_movk_i32 s16, 0x80
	ds_write_b64 v64, v[8:9] offset:0x4000
	v_xad_u32 v205, v36, s16, v32
	s_movk_i32 s16, 0xa0
	ds_write_b64 v65, v[10:11] offset:0x4000
	s_add_u32 s8, s6, 0x100
	v_xad_u32 v206, v36, s16, v32
	s_movk_i32 s16, 0xc0
	ds_write_b64 v66, v[0:1] offset:0x4000
	s_addc_u32 s9, s7, 0
	v_xad_u32 v207, v36, s16, v32
	s_movk_i32 s16, 0xe0
	ds_write_b64 v67, v[2:3] offset:0x4000
	v_add_u32_e32 v201, v32, v36
	v_xad_u32 v202, v36, 32, v32
	v_xad_u32 v203, v36, 64, v32
	v_xad_u32 v208, v36, s16, v32
	v_lshl_add_u32 v32, v143, 7, s10
	s_add_u32 s10, s78, 0x20000
	global_load_dwordx4 v[132:135], v198, s[8:9]
	s_addc_u32 s11, s79, 0
	global_load_dwordx4 v[128:131], v199, s[8:9]
	v_lshrrev_b32_e32 v34, 1, v137
	global_load_dwordx4 v[136:139], v196, s[10:11]
	s_add_u32 s6, s6, 0x180
	v_bitop3_b32 v34, v140, v34, 7 bitop3:0x78
	v_bitop3_b32 v37, v140, v35, 2 bitop3:0x36
	v_bitop3_b32 v38, v140, v35, 4 bitop3:0x36
	v_bitop3_b32 v35, v140, v35, 6 bitop3:0x36
	global_load_dwordx4 v[140:143], v197, s[10:11]
	s_addc_u32 s7, s7, 0
	s_add_u32 s8, s78, 0x30000
	global_load_dwordx4 v[148:151], v198, s[6:7]
	s_addc_u32 s9, s79, 0
	global_load_dwordx4 v[144:147], v199, s[6:7]
	global_load_dwordx4 v[152:155], v196, s[8:9]
	s_add_u32 s10, s13, s14
	global_load_dwordx4 v[156:159], v197, s[8:9]
	s_addc_u32 s11, s12, 0
	s_add_u32 s12, s41, s30
	v_mov_b32_e32 v0, 0
	s_mov_b32 s4, 0
	v_lshl_add_u32 v209, v34, 4, v32
	v_lshl_add_u32 v210, v37, 4, v32
	v_lshl_add_u32 v211, v38, 4, v32
	v_lshl_add_u32 v224, v35, 4, v32
	s_addc_u32 s13, 0, s31
	v_mov_b32_e32 v1, v0
	v_mov_b32_e32 v2, v0
	v_mov_b32_e32 v3, v0
	v_mov_b32_e32 v4, v0
	v_mov_b32_e32 v5, v0
	v_mov_b32_e32 v6, v0
	v_mov_b32_e32 v7, v0
	v_mov_b32_e32 v8, v0
	v_mov_b32_e32 v9, v0
	v_mov_b32_e32 v10, v0
	v_mov_b32_e32 v11, v0
	v_mov_b32_e32 v12, v0
	v_mov_b32_e32 v13, v0
	v_mov_b32_e32 v14, v0
	v_mov_b32_e32 v15, v0
	v_mov_b32_e32 v16, v0
	v_mov_b32_e32 v17, v0
	v_mov_b32_e32 v18, v0
	v_mov_b32_e32 v19, v0
	v_mov_b32_e32 v20, v0
	v_mov_b32_e32 v21, v0
	v_mov_b32_e32 v22, v0
	v_mov_b32_e32 v23, v0
	v_mov_b32_e32 v24, v0
	v_mov_b32_e32 v25, v0
	v_mov_b32_e32 v26, v0
	v_mov_b32_e32 v27, v0
	v_mov_b32_e32 v28, v0
	v_mov_b32_e32 v29, v0
	v_mov_b32_e32 v30, v0
	v_mov_b32_e32 v31, v0
	v_mov_b32_e32 v32, v0
	v_mov_b32_e32 v33, v0
	v_mov_b32_e32 v34, v0
	v_mov_b32_e32 v35, v0
	v_mov_b32_e32 v36, v0
	v_mov_b32_e32 v37, v0
	v_mov_b32_e32 v38, v0
	v_mov_b32_e32 v39, v0
	v_mov_b32_e32 v40, v0
	v_mov_b32_e32 v41, v0
	v_mov_b32_e32 v42, v0
	v_mov_b32_e32 v43, v0
	v_mov_b32_e32 v44, v0
	v_mov_b32_e32 v45, v0
	v_mov_b32_e32 v46, v0
	v_mov_b32_e32 v47, v0
	v_mov_b32_e32 v48, v0
	v_mov_b32_e32 v49, v0
	v_mov_b32_e32 v50, v0
	v_mov_b32_e32 v51, v0
	v_mov_b32_e32 v52, v0
	v_mov_b32_e32 v53, v0
	v_mov_b32_e32 v54, v0
	v_mov_b32_e32 v55, v0
	v_mov_b32_e32 v56, v0
	v_mov_b32_e32 v57, v0
	v_mov_b32_e32 v58, v0
	v_mov_b32_e32 v59, v0
	v_mov_b32_e32 v60, v0
	v_mov_b32_e32 v61, v0
	v_mov_b32_e32 v62, v0
	v_mov_b32_e32 v63, v0
	v_mov_b32_e32 v160, v0
	v_mov_b32_e32 v161, v0
	v_mov_b32_e32 v227, v64
	v_mov_b32_e32 v228, v65
	v_mov_b32_e32 v229, v66
	v_mov_b32_e32 v184, v67
	v_readlane_b32 s100, v250, 8
	v_mbcnt_lo_u32_b32 v68, -1, 0
	v_mbcnt_hi_u32_b32 v68, -1, v68
	v_and_b32_e32 v69, 15, v68
	v_lshrrev_b32_e32 v70, 4, v68
	v_lshlrev_b32_e32 v72, 8, v69
	v_add_u32_e32 v72, 0x10000, v72
	v_add_u32_e32 v71, 0, v70
	v_xor_b32_e32 v71, v71, v69
	v_lshl_add_u32 v201, v71, 4, v72
	v_add_u32_e32 v71, 4, v70
	v_xor_b32_e32 v71, v71, v69
	v_lshl_add_u32 v202, v71, 4, v72
	v_add_u32_e32 v71, 8, v70
	v_xor_b32_e32 v71, v71, v69
	v_lshl_add_u32 v203, v71, 4, v72
	v_add_u32_e32 v71, 12, v70
	v_xor_b32_e32 v71, v71, v69
	v_lshl_add_u32 v246, v71, 4, v72
	v_bfe_u32 v73, v69, 1, 3
	v_lshlrev_b32_e32 v76, 7, v69
	v_add_u32_e32 v71, 0, v70
	v_xor_b32_e32 v71, v71, v73
	v_lshl_add_u32 v209, v71, 4, v76
	v_add_u32_e32 v71, 4, v70
	v_xor_b32_e32 v71, v71, v73
	v_lshl_add_u32 v210, v71, 4, v76
	s_lshl_b32 s101, s100, 7
	s_add_u32 s101, s101, 0x8000
	s_cmpk_ge_u32 s100, 0x100
	s_cselect_b32 s6, 0x8000, 0
	s_add_u32 s101, s101, s6
	v_and_b32_e32 v74, 31, v68
	v_lshrrev_b32_e32 v75, 5, v68
	v_lshlrev_b32_e32 v74, 8, v74
	v_lshl_add_u32 v74, v75, 4, v74
	v_add_u32_e32 v74, s101, v74
	v_lshlrev_b32_e32 v75, 8, v69
	v_lshl_add_u32 v75, v70, 4, v75
	v_add_u32_e32 v75, s101, v75
	ds_write_b128 v74, v[96:99] offset:0
	ds_write_b128 v74, v[100:103] offset:32
	ds_write_b128 v74, v[104:107] offset:64
	ds_write_b128 v74, v[108:111] offset:96
	ds_write_b128 v74, v[112:115] offset:128
	ds_write_b128 v74, v[116:119] offset:160
	ds_write_b128 v74, v[120:123] offset:192
	ds_write_b128 v74, v[124:127] offset:224
	s_waitcnt lgkmcnt(0)
	ds_read_b128 v[96:99], v75 offset:0
	ds_read_b128 v[100:103], v75 offset:64
	ds_read_b128 v[104:107], v75 offset:128
	ds_read_b128 v[108:111], v75 offset:192
	ds_read_b128 v[112:115], v75 offset:4096
	ds_read_b128 v[116:119], v75 offset:4160
	ds_read_b128 v[120:123], v75 offset:4224
	ds_read_b128 v[124:127], v75 offset:4288
	s_waitcnt vmcnt(0)
	s_waitcnt lgkmcnt(0)
	s_barrier
	ds_write_b128 v225, v[136:139] offset:32768
	ds_write_b128 v226, v[140:143] offset:32768
	s_add_u32 s15, s22, s12
	s_addc_u32 s14, s23, s13
	s_add_u32 s6, s15, 0x23a40000
	s_addc_u32 s7, s14, 0
	s_waitcnt lgkmcnt(0)
	global_load_dwordx4 v[136:139], v196, s[6:7]
	global_load_dwordx4 v[140:143], v197, s[6:7]
	v_mov_b32_e32 v194, 0
	v_mov_b32_e32 v195, 0
	s_barrier
	ds_read_b128 v[160:163], v201 offset:0
	ds_read_b128 v[164:167], v202 offset:0
	ds_read_b128 v[168:171], v203 offset:0
	ds_read_b128 v[172:175], v246 offset:0
	ds_read_b128 v[176:179], v201 offset:4096
	ds_read_b128 v[180:183], v202 offset:4096
	ds_read_b128 v[230:233], v203 offset:4096
	s_waitcnt lgkmcnt(6)
	v_mfma_f32_16x16x32_bf16 v[64:67], v[160:163], v[96:99], 0
	v_mfma_f32_16x16x32_bf16 v[68:71], v[160:163], v[112:115], 0
	ds_read_b128 v[234:237], v246 offset:4096
	s_waitcnt lgkmcnt(6)
	v_mfma_f32_16x16x32_bf16 v[68:71], v[164:167], v[116:119], v[68:71]
	v_mfma_f32_16x16x32_bf16 v[64:67], v[164:167], v[100:103], v[64:67]
	ds_read_b128 v[160:163], v201 offset:8192
	s_waitcnt lgkmcnt(6)
	v_mfma_f32_16x16x32_bf16 v[64:67], v[168:171], v[104:107], v[64:67]
	v_mfma_f32_16x16x32_bf16 v[68:71], v[168:171], v[120:123], v[68:71]
	ds_read_b128 v[164:167], v202 offset:8192
	s_waitcnt lgkmcnt(6)
	v_mfma_f32_16x16x32_bf16 v[68:71], v[172:175], v[124:127], v[68:71]
	v_mfma_f32_16x16x32_bf16 v[64:67], v[172:175], v[108:111], v[64:67]
	ds_read_b128 v[168:171], v203 offset:8192
	s_waitcnt lgkmcnt(6)
	v_mfma_f32_16x16x32_bf16 v[72:75], v[176:179], v[96:99], 0
	s_nop 7
	s_nop 1
	v_exp_f32_e32 v64, v64
	v_mfma_f32_16x16x32_bf16 v[76:79], v[176:179], v[112:115], 0
	v_exp_f32_e32 v68, v68
	ds_read_b128 v[172:175], v246 offset:8192
	s_waitcnt lgkmcnt(6)
	v_mfma_f32_16x16x32_bf16 v[76:79], v[180:183], v[116:119], v[76:79]
	v_exp_f32_e32 v65, v65
	v_exp_f32_e32 v69, v69
	v_mfma_f32_16x16x32_bf16 v[72:75], v[180:183], v[100:103], v[72:75]
	v_exp_f32_e32 v66, v66
	ds_read_b128 v[176:179], v201 offset:12288
	s_waitcnt lgkmcnt(6)
	v_mfma_f32_16x16x32_bf16 v[72:75], v[230:233], v[104:107], v[72:75]
	v_exp_f32_e32 v70, v70
	v_exp_f32_e32 v67, v67
	v_mfma_f32_16x16x32_bf16 v[76:79], v[230:233], v[120:123], v[76:79]
	v_exp_f32_e32 v71, v71
	v_add_f32_e32 v220, v64, v65
	ds_read_b128 v[180:183], v202 offset:12288
	s_waitcnt lgkmcnt(6)
	v_mfma_f32_16x16x32_bf16 v[76:79], v[234:237], v[124:127], v[76:79]
	v_add_f32_e32 v221, v68, v69
	v_add_f32_e32 v220, v220, v66
	v_add_f32_e32 v221, v221, v70
	v_mfma_f32_16x16x32_bf16 v[72:75], v[234:237], v[108:111], v[72:75]
	v_add_f32_e32 v220, v220, v67
	v_add_f32_e32 v221, v221, v71
	ds_read_b128 v[230:233], v203 offset:12288
	s_waitcnt lgkmcnt(6)
	v_mfma_f32_16x16x32_bf16 v[80:83], v[160:163], v[96:99], 0
	s_nop 7
	s_nop 1
	v_exp_f32_e32 v72, v72
	v_exp_f32_e32 v76, v76
	v_mfma_f32_16x16x32_bf16 v[84:87], v[160:163], v[112:115], 0
	v_exp_f32_e32 v73, v73
	v_exp_f32_e32 v77, v77
	ds_read_b128 v[234:237], v246 offset:12288
	s_waitcnt lgkmcnt(6)
	v_mfma_f32_16x16x32_bf16 v[84:87], v[164:167], v[116:119], v[84:87]
	v_exp_f32_e32 v74, v74
	v_exp_f32_e32 v78, v78
	v_mfma_f32_16x16x32_bf16 v[80:83], v[164:167], v[100:103], v[80:83]
	v_exp_f32_e32 v75, v75
	v_exp_f32_e32 v79, v79
	s_waitcnt lgkmcnt(5)
	v_mfma_f32_16x16x32_bf16 v[80:83], v[168:171], v[104:107], v[80:83]
	v_add_f32_e32 v220, v220, v72
	v_add_f32_e32 v221, v221, v76
	v_add_f32_e32 v220, v220, v73
	v_add_f32_e32 v221, v221, v77
	v_mfma_f32_16x16x32_bf16 v[84:87], v[168:171], v[120:123], v[84:87]
	v_add_f32_e32 v220, v220, v74
	v_add_f32_e32 v221, v221, v78
	v_add_f32_e32 v220, v220, v75
	v_add_f32_e32 v221, v221, v79
	s_waitcnt lgkmcnt(4)
	v_mfma_f32_16x16x32_bf16 v[84:87], v[172:175], v[124:127], v[84:87]
	v_cvt_pk_bf16_f32 v216, v64, v65
	v_cvt_pk_bf16_f32 v217, v66, v67
	v_cvt_pk_bf16_f32 v238, v68, v69
	v_cvt_pk_bf16_f32 v239, v70, v71
	v_mfma_f32_16x16x32_bf16 v[80:83], v[172:175], v[108:111], v[80:83]
	v_cvt_pk_bf16_f32 v218, v72, v73
	v_cvt_pk_bf16_f32 v219, v74, v75
	v_cvt_pk_bf16_f32 v240, v76, v77
	v_cvt_pk_bf16_f32 v241, v78, v79
	s_waitcnt lgkmcnt(3)
	v_mfma_f32_16x16x32_bf16 v[88:91], v[176:179], v[96:99], 0
	s_nop 7
	s_nop 1
	v_exp_f32_e32 v80, v80
	v_exp_f32_e32 v84, v84
	v_mfma_f32_16x16x32_bf16 v[92:95], v[176:179], v[112:115], 0
	v_exp_f32_e32 v81, v81
	s_waitcnt lgkmcnt(2)
	v_mfma_f32_16x16x32_bf16 v[92:95], v[180:183], v[116:119], v[92:95]
	v_exp_f32_e32 v85, v85
	v_exp_f32_e32 v82, v82
	v_mfma_f32_16x16x32_bf16 v[88:91], v[180:183], v[100:103], v[88:91]
	v_exp_f32_e32 v86, v86
	s_waitcnt lgkmcnt(1)
	v_mfma_f32_16x16x32_bf16 v[88:91], v[230:233], v[104:107], v[88:91]
	v_exp_f32_e32 v83, v83
	v_exp_f32_e32 v87, v87
	v_mfma_f32_16x16x32_bf16 v[92:95], v[230:233], v[120:123], v[92:95]
	v_add_f32_e32 v220, v220, v80
	v_add_f32_e32 v221, v221, v84
	v_add_f32_e32 v220, v220, v81
	s_waitcnt lgkmcnt(0)
	v_mfma_f32_16x16x32_bf16 v[92:95], v[234:237], v[124:127], v[92:95]
	v_add_f32_e32 v221, v221, v85
	v_add_f32_e32 v220, v220, v82
	v_add_f32_e32 v221, v221, v86
	v_mfma_f32_16x16x32_bf16 v[88:91], v[234:237], v[108:111], v[88:91]
	v_add_f32_e32 v220, v220, v83
	v_add_f32_e32 v221, v221, v87
	s_waitcnt lgkmcnt(0)
	s_barrier
	ds_read_b128 v[160:163], v201 offset:16384
	ds_read_b128 v[164:167], v209 offset:0
	ds_read_b128 v[168:171], v202 offset:16384
	ds_read_b128 v[172:175], v209 offset:2048
	ds_read_b128 v[176:179], v203 offset:16384
	ds_read_b128 v[180:183], v209 offset:4096
	ds_read_b128 v[230:233], v246 offset:16384
.LBB0_734:
	s_waitcnt lgkmcnt(6)
	v_mfma_f32_16x16x32_bf16 v[64:67], v[160:163], v[96:99], 0
	v_exp_f32_e32 v88, v88
	v_mfma_f32_16x16x32_bf16 v[68:71], v[160:163], v[112:115], 0
	v_exp_f32_e32 v92, v92
	ds_read_b128 v[234:237], v209 offset:6144
	s_add_u32 s16, s22, s10
	s_addc_u32 s17, s23, s11
	s_add_u32 s15, s22, s12
	s_addc_u32 s14, s23, s13
	s_add_u32 s8, s16, 0x3bc00200
	s_addc_u32 s9, s17, 0
	s_add_u32 s6, s15, 0x23a50000
	s_addc_u32 s7, s14, 0
	s_waitcnt lgkmcnt(6)
	v_mfma_f32_16x16x32_bf16 v[0:3], v[164:167], v[216:219], v[0:3]
	v_cvt_pk_bf16_f32 v242, v80, v81
	v_mfma_f32_16x16x32_bf16 v[4:7], v[164:167], v[238:241], v[4:7]
	v_exp_f32_e32 v89, v89
	ds_read_b128 v[160:163], v201 offset:20480
	s_waitcnt vmcnt(4)
	ds_write_b128 v225, v[152:155] offset:49152
	s_waitcnt lgkmcnt(7)
	v_mfma_f32_16x16x32_bf16 v[68:71], v[168:171], v[116:119], v[68:71]
	v_exp_f32_e32 v93, v93
	v_mfma_f32_16x16x32_bf16 v[64:67], v[168:171], v[100:103], v[64:67]
	v_cvt_pk_bf16_f32 v243, v82, v83
	ds_read_b128 v[164:167], v209 offset:8192
	ds_write_b128 v226, v[156:159] offset:49152
	s_waitcnt lgkmcnt(8)
	v_mfma_f32_16x16x32_bf16 v[12:15], v[172:175], v[238:241], v[12:15]
	v_exp_f32_e32 v90, v90
	v_mfma_f32_16x16x32_bf16 v[8:11], v[172:175], v[216:219], v[8:11]
	v_exp_f32_e32 v94, v94
	ds_read_b128 v[168:171], v202 offset:20480
	ds_write_b64 v227, v[132:133] offset:32768
	s_waitcnt lgkmcnt(9)
	v_mfma_f32_16x16x32_bf16 v[64:67], v[176:179], v[104:107], v[64:67]
	v_cvt_pk_bf16_f32 v204, v84, v85
	v_mfma_f32_16x16x32_bf16 v[68:71], v[176:179], v[120:123], v[68:71]
	v_exp_f32_e32 v91, v91
	ds_read_b128 v[172:175], v209 offset:10240
	ds_write_b64 v228, v[134:135] offset:32768
	s_waitcnt lgkmcnt(10)
	v_mfma_f32_16x16x32_bf16 v[16:19], v[180:183], v[216:219], v[16:19]
	v_exp_f32_e32 v95, v95
	v_mfma_f32_16x16x32_bf16 v[20:23], v[180:183], v[238:241], v[20:23]
	v_cvt_pk_bf16_f32 v205, v86, v87
	v_add_f32_e32 v220, v220, v88
	ds_read_b128 v[176:179], v203 offset:20480
	ds_write_b64 v229, v[128:129] offset:32768
	s_waitcnt lgkmcnt(11)
	v_mfma_f32_16x16x32_bf16 v[68:71], v[230:233], v[124:127], v[68:71]
	v_add_f32_e32 v221, v221, v92
	v_add_f32_e32 v220, v220, v89
	v_mfma_f32_16x16x32_bf16 v[64:67], v[230:233], v[108:111], v[64:67]
	v_add_f32_e32 v221, v221, v93
	v_cvt_pk_bf16_f32 v244, v88, v89
	ds_read_b128 v[180:183], v209 offset:12288
	ds_write_b64 v184, v[130:131] offset:32768
	s_waitcnt lgkmcnt(12)
	v_mfma_f32_16x16x32_bf16 v[28:31], v[234:237], v[238:241], v[28:31]
	v_cvt_pk_bf16_f32 v245, v90, v91
	v_cvt_pk_bf16_f32 v206, v92, v93
	v_mfma_f32_16x16x32_bf16 v[24:27], v[234:237], v[216:219], v[24:27]
	v_cvt_pk_bf16_f32 v207, v94, v95
	ds_read_b128 v[230:233], v246 offset:20480
	global_load_dwordx4 v[132:135], v198, s[8:9]
	s_waitcnt lgkmcnt(12)
	v_mfma_f32_16x16x32_bf16 v[72:75], v[160:163], v[96:99], 0
	v_add_f32_e32 v220, v220, v90
	v_add_f32_e32 v221, v221, v94
	v_mfma_f32_16x16x32_bf16 v[76:79], v[160:163], v[112:115], 0
	v_add_f32_e32 v220, v220, v91
	v_add_f32_e32 v221, v221, v95
	ds_read_b128 v[234:237], v209 offset:14336
	global_load_dwordx4 v[128:131], v199, s[8:9]
	s_waitcnt lgkmcnt(11)
	v_mfma_f32_16x16x32_bf16 v[32:35], v[164:167], v[216:219], v[32:35]
	v_add_f32_e32 v194, v194, v220
	v_add_f32_e32 v195, v195, v221
	v_mfma_f32_16x16x32_bf16 v[36:39], v[164:167], v[238:241], v[36:39]
	v_exp_f32_e32 v64, v64
	ds_read_b128 v[160:163], v201 offset:24576
	global_load_dwordx4 v[152:155], v196, s[6:7]
	s_waitcnt lgkmcnt(10)
	v_mfma_f32_16x16x32_bf16 v[76:79], v[168:171], v[116:119], v[76:79]
	v_exp_f32_e32 v68, v68
	v_mfma_f32_16x16x32_bf16 v[72:75], v[168:171], v[100:103], v[72:75]
	v_exp_f32_e32 v65, v65
	ds_read_b128 v[164:167], v210 offset:0
	global_load_dwordx4 v[156:159], v197, s[6:7]
	s_waitcnt lgkmcnt(9)
	v_mfma_f32_16x16x32_bf16 v[44:47], v[172:175], v[238:241], v[44:47]
	v_exp_f32_e32 v69, v69
	v_mfma_f32_16x16x32_bf16 v[40:43], v[172:175], v[216:219], v[40:43]
	v_exp_f32_e32 v66, v66
	ds_read_b128 v[168:171], v202 offset:24576
	s_waitcnt lgkmcnt(8)
	v_mfma_f32_16x16x32_bf16 v[72:75], v[176:179], v[104:107], v[72:75]
	v_exp_f32_e32 v70, v70
	v_mfma_f32_16x16x32_bf16 v[76:79], v[176:179], v[120:123], v[76:79]
	v_exp_f32_e32 v67, v67
	ds_read_b128 v[172:175], v210 offset:2048
	s_waitcnt lgkmcnt(7)
	v_mfma_f32_16x16x32_bf16 v[48:51], v[180:183], v[216:219], v[48:51]
	v_exp_f32_e32 v71, v71
	v_mfma_f32_16x16x32_bf16 v[52:55], v[180:183], v[238:241], v[52:55]
	v_add_f32_e32 v220, v64, v65
	ds_read_b128 v[176:179], v203 offset:24576
	s_waitcnt lgkmcnt(6)
	v_mfma_f32_16x16x32_bf16 v[76:79], v[230:233], v[124:127], v[76:79]
	v_add_f32_e32 v221, v68, v69
	v_mfma_f32_16x16x32_bf16 v[72:75], v[230:233], v[108:111], v[72:75]
	v_add_f32_e32 v220, v220, v66
	ds_read_b128 v[180:183], v210 offset:4096
	s_waitcnt lgkmcnt(6)
	v_mfma_f32_16x16x32_bf16 v[60:63], v[234:237], v[238:241], v[60:63]
	v_add_f32_e32 v221, v221, v70
	v_add_f32_e32 v220, v220, v67
	v_mfma_f32_16x16x32_bf16 v[56:59], v[234:237], v[216:219], v[56:59]
	v_add_f32_e32 v221, v221, v71
	ds_read_b128 v[230:233], v246 offset:24576
	s_waitcnt lgkmcnt(6)
	v_mfma_f32_16x16x32_bf16 v[80:83], v[160:163], v[96:99], 0
	v_exp_f32_e32 v72, v72
	v_mfma_f32_16x16x32_bf16 v[84:87], v[160:163], v[112:115], 0
	v_exp_f32_e32 v76, v76
	ds_read_b128 v[234:237], v210 offset:6144
	s_waitcnt lgkmcnt(6)
	v_mfma_f32_16x16x32_bf16 v[0:3], v[164:167], v[242:245], v[0:3]
	v_exp_f32_e32 v73, v73
	v_mfma_f32_16x16x32_bf16 v[4:7], v[164:167], v[204:207], v[4:7]
	v_exp_f32_e32 v77, v77
	ds_read_b128 v[160:163], v201 offset:28672
	s_waitcnt lgkmcnt(6)
	v_mfma_f32_16x16x32_bf16 v[84:87], v[168:171], v[116:119], v[84:87]
	v_exp_f32_e32 v74, v74
	v_mfma_f32_16x16x32_bf16 v[80:83], v[168:171], v[100:103], v[80:83]
	v_exp_f32_e32 v78, v78
	ds_read_b128 v[164:167], v210 offset:8192
	s_waitcnt lgkmcnt(6)
	v_mfma_f32_16x16x32_bf16 v[12:15], v[172:175], v[204:207], v[12:15]
	v_exp_f32_e32 v75, v75
	v_mfma_f32_16x16x32_bf16 v[8:11], v[172:175], v[242:245], v[8:11]
	v_exp_f32_e32 v79, v79
	ds_read_b128 v[168:171], v202 offset:28672
	s_waitcnt lgkmcnt(6)
	v_mfma_f32_16x16x32_bf16 v[80:83], v[176:179], v[104:107], v[80:83]
	v_add_f32_e32 v220, v220, v72
	v_add_f32_e32 v221, v221, v76
	v_mfma_f32_16x16x32_bf16 v[84:87], v[176:179], v[120:123], v[84:87]
	v_add_f32_e32 v220, v220, v73
	ds_read_b128 v[172:175], v210 offset:10240
	s_waitcnt lgkmcnt(6)
	v_mfma_f32_16x16x32_bf16 v[16:19], v[180:183], v[242:245], v[16:19]
	v_add_f32_e32 v221, v221, v77
	v_add_f32_e32 v220, v220, v74
	v_mfma_f32_16x16x32_bf16 v[20:23], v[180:183], v[204:207], v[20:23]
	v_add_f32_e32 v221, v221, v78
	ds_read_b128 v[176:179], v203 offset:28672
	s_waitcnt lgkmcnt(6)
	v_mfma_f32_16x16x32_bf16 v[84:87], v[230:233], v[124:127], v[84:87]
	v_add_f32_e32 v220, v220, v75
	v_add_f32_e32 v221, v221, v79
	v_mfma_f32_16x16x32_bf16 v[80:83], v[230:233], v[108:111], v[80:83]
	v_cvt_pk_bf16_f32 v216, v64, v65
	ds_read_b128 v[180:183], v210 offset:12288
	s_waitcnt lgkmcnt(6)
	v_mfma_f32_16x16x32_bf16 v[28:31], v[234:237], v[204:207], v[28:31]
	v_cvt_pk_bf16_f32 v217, v66, v67
	v_cvt_pk_bf16_f32 v238, v68, v69
	v_mfma_f32_16x16x32_bf16 v[24:27], v[234:237], v[242:245], v[24:27]
	v_cvt_pk_bf16_f32 v239, v70, v71
	ds_read_b128 v[230:233], v246 offset:28672
	s_waitcnt lgkmcnt(6)
	v_mfma_f32_16x16x32_bf16 v[88:91], v[160:163], v[96:99], 0
	v_exp_f32_e32 v80, v80
	v_mfma_f32_16x16x32_bf16 v[92:95], v[160:163], v[112:115], 0
	v_exp_f32_e32 v84, v84
	ds_read_b128 v[234:237], v210 offset:14336
	s_waitcnt lgkmcnt(6)
	v_mfma_f32_16x16x32_bf16 v[32:35], v[164:167], v[242:245], v[32:35]
	v_exp_f32_e32 v81, v81
	v_mfma_f32_16x16x32_bf16 v[36:39], v[164:167], v[204:207], v[36:39]
	v_exp_f32_e32 v85, v85
	ds_read_b128 v[160:163], v201 offset:32768
	s_waitcnt lgkmcnt(6)
	v_mfma_f32_16x16x32_bf16 v[92:95], v[168:171], v[116:119], v[92:95]
	v_exp_f32_e32 v82, v82
	v_mfma_f32_16x16x32_bf16 v[88:91], v[168:171], v[100:103], v[88:91]
	v_exp_f32_e32 v86, v86
	ds_read_b128 v[164:167], v209 offset:16384
	s_waitcnt lgkmcnt(6)
	v_mfma_f32_16x16x32_bf16 v[44:47], v[172:175], v[204:207], v[44:47]
	v_exp_f32_e32 v83, v83
	v_mfma_f32_16x16x32_bf16 v[40:43], v[172:175], v[242:245], v[40:43]
	v_exp_f32_e32 v87, v87
	ds_read_b128 v[168:171], v202 offset:32768
	s_waitcnt lgkmcnt(6)
	v_mfma_f32_16x16x32_bf16 v[88:91], v[176:179], v[104:107], v[88:91]
	v_add_f32_e32 v220, v220, v80
	v_add_f32_e32 v221, v221, v84
	v_mfma_f32_16x16x32_bf16 v[92:95], v[176:179], v[120:123], v[92:95]
	v_add_f32_e32 v220, v220, v81
	ds_read_b128 v[172:175], v209 offset:18432
	s_waitcnt lgkmcnt(6)
	v_mfma_f32_16x16x32_bf16 v[48:51], v[180:183], v[242:245], v[48:51]
	v_add_f32_e32 v221, v221, v85
	v_add_f32_e32 v220, v220, v82
	v_mfma_f32_16x16x32_bf16 v[52:55], v[180:183], v[204:207], v[52:55]
	v_add_f32_e32 v221, v221, v86
	ds_read_b128 v[176:179], v203 offset:32768
	s_waitcnt lgkmcnt(6)
	v_mfma_f32_16x16x32_bf16 v[92:95], v[230:233], v[124:127], v[92:95]
	v_add_f32_e32 v220, v220, v83
	v_add_f32_e32 v221, v221, v87
	v_mfma_f32_16x16x32_bf16 v[88:91], v[230:233], v[108:111], v[88:91]
	v_cvt_pk_bf16_f32 v218, v72, v73
	ds_read_b128 v[180:183], v209 offset:20480
	s_waitcnt lgkmcnt(6)
	v_mfma_f32_16x16x32_bf16 v[60:63], v[234:237], v[204:207], v[60:63]
	v_cvt_pk_bf16_f32 v219, v74, v75
	v_cvt_pk_bf16_f32 v240, v76, v77
	v_mfma_f32_16x16x32_bf16 v[56:59], v[234:237], v[242:245], v[56:59]
	v_cvt_pk_bf16_f32 v241, v78, v79
	ds_read_b128 v[230:233], v246 offset:32768
	s_waitcnt lgkmcnt(6)
	v_mfma_f32_16x16x32_bf16 v[64:67], v[160:163], v[96:99], 0
	v_exp_f32_e32 v88, v88
	v_mfma_f32_16x16x32_bf16 v[68:71], v[160:163], v[112:115], 0
	v_exp_f32_e32 v92, v92
	ds_read_b128 v[234:237], v209 offset:22528
	s_add_u32 s8, s16, 0x3bc00280
	s_addc_u32 s9, s17, 0
	s_add_u32 s6, s15, 0x23a60000
	s_addc_u32 s7, s14, 0
	s_waitcnt lgkmcnt(6)
	v_mfma_f32_16x16x32_bf16 v[0:3], v[164:167], v[216:219], v[0:3]
	v_cvt_pk_bf16_f32 v242, v80, v81
	v_mfma_f32_16x16x32_bf16 v[4:7], v[164:167], v[238:241], v[4:7]
	v_exp_f32_e32 v89, v89
	ds_read_b128 v[160:163], v201 offset:36864
	s_waitcnt vmcnt(4)
	ds_write_b128 v225, v[136:139] offset:0
	s_waitcnt lgkmcnt(7)
	v_mfma_f32_16x16x32_bf16 v[68:71], v[168:171], v[116:119], v[68:71]
	v_exp_f32_e32 v93, v93
	v_mfma_f32_16x16x32_bf16 v[64:67], v[168:171], v[100:103], v[64:67]
	v_cvt_pk_bf16_f32 v243, v82, v83
	ds_read_b128 v[164:167], v209 offset:24576
	ds_write_b128 v226, v[140:143] offset:0
	s_waitcnt lgkmcnt(8)
	v_mfma_f32_16x16x32_bf16 v[12:15], v[172:175], v[238:241], v[12:15]
	v_exp_f32_e32 v90, v90
	v_mfma_f32_16x16x32_bf16 v[8:11], v[172:175], v[216:219], v[8:11]
	v_exp_f32_e32 v94, v94
	ds_read_b128 v[168:171], v202 offset:36864
	ds_write_b64 v227, v[148:149] offset:49152
	s_waitcnt lgkmcnt(9)
	v_mfma_f32_16x16x32_bf16 v[64:67], v[176:179], v[104:107], v[64:67]
	v_cvt_pk_bf16_f32 v204, v84, v85
	v_mfma_f32_16x16x32_bf16 v[68:71], v[176:179], v[120:123], v[68:71]
	v_exp_f32_e32 v91, v91
	ds_read_b128 v[172:175], v209 offset:26624
	ds_write_b64 v228, v[150:151] offset:49152
	s_waitcnt lgkmcnt(10)
	v_mfma_f32_16x16x32_bf16 v[16:19], v[180:183], v[216:219], v[16:19]
	v_exp_f32_e32 v95, v95
	v_mfma_f32_16x16x32_bf16 v[20:23], v[180:183], v[238:241], v[20:23]
	v_cvt_pk_bf16_f32 v205, v86, v87
	v_add_f32_e32 v220, v220, v88
	ds_read_b128 v[176:179], v203 offset:36864
	ds_write_b64 v229, v[144:145] offset:49152
	s_waitcnt lgkmcnt(11)
	v_mfma_f32_16x16x32_bf16 v[68:71], v[230:233], v[124:127], v[68:71]
	v_add_f32_e32 v221, v221, v92
	v_add_f32_e32 v220, v220, v89
	v_mfma_f32_16x16x32_bf16 v[64:67], v[230:233], v[108:111], v[64:67]
	v_add_f32_e32 v221, v221, v93
	v_cvt_pk_bf16_f32 v244, v88, v89
	ds_read_b128 v[180:183], v209 offset:28672
	ds_write_b64 v184, v[146:147] offset:49152
	s_waitcnt lgkmcnt(12)
	v_mfma_f32_16x16x32_bf16 v[28:31], v[234:237], v[238:241], v[28:31]
	v_cvt_pk_bf16_f32 v245, v90, v91
	v_cvt_pk_bf16_f32 v206, v92, v93
	v_mfma_f32_16x16x32_bf16 v[24:27], v[234:237], v[216:219], v[24:27]
	v_cvt_pk_bf16_f32 v207, v94, v95
	ds_read_b128 v[230:233], v246 offset:36864
	global_load_dwordx4 v[148:151], v198, s[8:9]
	s_waitcnt lgkmcnt(12)
	v_mfma_f32_16x16x32_bf16 v[72:75], v[160:163], v[96:99], 0
	v_add_f32_e32 v220, v220, v90
	v_add_f32_e32 v221, v221, v94
	v_mfma_f32_16x16x32_bf16 v[76:79], v[160:163], v[112:115], 0
	v_add_f32_e32 v220, v220, v91
	v_add_f32_e32 v221, v221, v95
	ds_read_b128 v[234:237], v209 offset:30720
	global_load_dwordx4 v[144:147], v199, s[8:9]
	s_waitcnt lgkmcnt(11)
	v_mfma_f32_16x16x32_bf16 v[32:35], v[164:167], v[216:219], v[32:35]
	v_add_f32_e32 v194, v194, v220
	v_add_f32_e32 v195, v195, v221
	v_mfma_f32_16x16x32_bf16 v[36:39], v[164:167], v[238:241], v[36:39]
	v_exp_f32_e32 v64, v64
	ds_read_b128 v[160:163], v201 offset:40960
	global_load_dwordx4 v[136:139], v196, s[6:7]
	s_waitcnt lgkmcnt(10)
	v_mfma_f32_16x16x32_bf16 v[76:79], v[168:171], v[116:119], v[76:79]
	v_exp_f32_e32 v68, v68
	v_mfma_f32_16x16x32_bf16 v[72:75], v[168:171], v[100:103], v[72:75]
	v_exp_f32_e32 v65, v65
	ds_read_b128 v[164:167], v210 offset:16384
	global_load_dwordx4 v[140:143], v197, s[6:7]
	s_waitcnt lgkmcnt(9)
	v_mfma_f32_16x16x32_bf16 v[44:47], v[172:175], v[238:241], v[44:47]
	v_exp_f32_e32 v69, v69
	v_mfma_f32_16x16x32_bf16 v[40:43], v[172:175], v[216:219], v[40:43]
	v_exp_f32_e32 v66, v66
	ds_read_b128 v[168:171], v202 offset:40960
	s_waitcnt lgkmcnt(8)
	v_mfma_f32_16x16x32_bf16 v[72:75], v[176:179], v[104:107], v[72:75]
	v_exp_f32_e32 v70, v70
	v_mfma_f32_16x16x32_bf16 v[76:79], v[176:179], v[120:123], v[76:79]
	v_exp_f32_e32 v67, v67
	ds_read_b128 v[172:175], v210 offset:18432
	s_waitcnt lgkmcnt(7)
	v_mfma_f32_16x16x32_bf16 v[48:51], v[180:183], v[216:219], v[48:51]
	v_exp_f32_e32 v71, v71
	v_mfma_f32_16x16x32_bf16 v[52:55], v[180:183], v[238:241], v[52:55]
	v_add_f32_e32 v220, v64, v65
	ds_read_b128 v[176:179], v203 offset:40960
	s_waitcnt lgkmcnt(6)
	v_mfma_f32_16x16x32_bf16 v[76:79], v[230:233], v[124:127], v[76:79]
	v_add_f32_e32 v221, v68, v69
	v_mfma_f32_16x16x32_bf16 v[72:75], v[230:233], v[108:111], v[72:75]
	v_add_f32_e32 v220, v220, v66
	ds_read_b128 v[180:183], v210 offset:20480
	s_waitcnt lgkmcnt(6)
	v_mfma_f32_16x16x32_bf16 v[60:63], v[234:237], v[238:241], v[60:63]
	v_add_f32_e32 v221, v221, v70
	v_add_f32_e32 v220, v220, v67
	v_mfma_f32_16x16x32_bf16 v[56:59], v[234:237], v[216:219], v[56:59]
	v_add_f32_e32 v221, v221, v71
	ds_read_b128 v[230:233], v246 offset:40960
	s_waitcnt lgkmcnt(6)
	v_mfma_f32_16x16x32_bf16 v[80:83], v[160:163], v[96:99], 0
	v_exp_f32_e32 v72, v72
	v_mfma_f32_16x16x32_bf16 v[84:87], v[160:163], v[112:115], 0
	v_exp_f32_e32 v76, v76
	ds_read_b128 v[234:237], v210 offset:22528
	s_waitcnt lgkmcnt(6)
	v_mfma_f32_16x16x32_bf16 v[0:3], v[164:167], v[242:245], v[0:3]
	v_exp_f32_e32 v73, v73
	v_mfma_f32_16x16x32_bf16 v[4:7], v[164:167], v[204:207], v[4:7]
	v_exp_f32_e32 v77, v77
	ds_read_b128 v[160:163], v201 offset:45056
	s_waitcnt lgkmcnt(6)
	v_mfma_f32_16x16x32_bf16 v[84:87], v[168:171], v[116:119], v[84:87]
	v_exp_f32_e32 v74, v74
	v_mfma_f32_16x16x32_bf16 v[80:83], v[168:171], v[100:103], v[80:83]
	v_exp_f32_e32 v78, v78
	ds_read_b128 v[164:167], v210 offset:24576
	s_waitcnt lgkmcnt(6)
	v_mfma_f32_16x16x32_bf16 v[12:15], v[172:175], v[204:207], v[12:15]
	v_exp_f32_e32 v75, v75
	v_mfma_f32_16x16x32_bf16 v[8:11], v[172:175], v[242:245], v[8:11]
	v_exp_f32_e32 v79, v79
	ds_read_b128 v[168:171], v202 offset:45056
	s_waitcnt lgkmcnt(6)
	v_mfma_f32_16x16x32_bf16 v[80:83], v[176:179], v[104:107], v[80:83]
	v_add_f32_e32 v220, v220, v72
	v_add_f32_e32 v221, v221, v76
	v_mfma_f32_16x16x32_bf16 v[84:87], v[176:179], v[120:123], v[84:87]
	v_add_f32_e32 v220, v220, v73
	ds_read_b128 v[172:175], v210 offset:26624
	s_waitcnt lgkmcnt(6)
	v_mfma_f32_16x16x32_bf16 v[16:19], v[180:183], v[242:245], v[16:19]
	v_add_f32_e32 v221, v221, v77
	v_add_f32_e32 v220, v220, v74
	v_mfma_f32_16x16x32_bf16 v[20:23], v[180:183], v[204:207], v[20:23]
	v_add_f32_e32 v221, v221, v78
	ds_read_b128 v[176:179], v203 offset:45056
	s_waitcnt lgkmcnt(6)
	v_mfma_f32_16x16x32_bf16 v[84:87], v[230:233], v[124:127], v[84:87]
	v_add_f32_e32 v220, v220, v75
	v_add_f32_e32 v221, v221, v79
	v_mfma_f32_16x16x32_bf16 v[80:83], v[230:233], v[108:111], v[80:83]
	v_cvt_pk_bf16_f32 v216, v64, v65
	ds_read_b128 v[180:183], v210 offset:28672
	s_waitcnt lgkmcnt(6)
	v_mfma_f32_16x16x32_bf16 v[28:31], v[234:237], v[204:207], v[28:31]
	v_cvt_pk_bf16_f32 v217, v66, v67
	v_cvt_pk_bf16_f32 v238, v68, v69
	v_mfma_f32_16x16x32_bf16 v[24:27], v[234:237], v[242:245], v[24:27]
	v_cvt_pk_bf16_f32 v239, v70, v71
	ds_read_b128 v[230:233], v246 offset:45056
	s_waitcnt lgkmcnt(6)
	v_mfma_f32_16x16x32_bf16 v[88:91], v[160:163], v[96:99], 0
	v_exp_f32_e32 v80, v80
	v_mfma_f32_16x16x32_bf16 v[92:95], v[160:163], v[112:115], 0
	v_exp_f32_e32 v84, v84
	ds_read_b128 v[234:237], v210 offset:30720
	s_waitcnt lgkmcnt(6)
	v_mfma_f32_16x16x32_bf16 v[32:35], v[164:167], v[242:245], v[32:35]
	v_exp_f32_e32 v81, v81
	v_mfma_f32_16x16x32_bf16 v[36:39], v[164:167], v[204:207], v[36:39]
	v_exp_f32_e32 v85, v85
	s_waitcnt lgkmcnt(5)
	v_mfma_f32_16x16x32_bf16 v[92:95], v[168:171], v[116:119], v[92:95]
	v_exp_f32_e32 v82, v82
	v_mfma_f32_16x16x32_bf16 v[88:91], v[168:171], v[100:103], v[88:91]
	v_exp_f32_e32 v86, v86
	s_waitcnt lgkmcnt(4)
	v_mfma_f32_16x16x32_bf16 v[44:47], v[172:175], v[204:207], v[44:47]
	v_exp_f32_e32 v83, v83
	v_mfma_f32_16x16x32_bf16 v[40:43], v[172:175], v[242:245], v[40:43]
	v_exp_f32_e32 v87, v87
	s_waitcnt lgkmcnt(3)
	v_mfma_f32_16x16x32_bf16 v[88:91], v[176:179], v[104:107], v[88:91]
	v_add_f32_e32 v220, v220, v80
	v_add_f32_e32 v221, v221, v84
	v_mfma_f32_16x16x32_bf16 v[92:95], v[176:179], v[120:123], v[92:95]
	v_add_f32_e32 v220, v220, v81
	s_waitcnt lgkmcnt(0)
	s_barrier
	ds_read_b128 v[160:163], v201 offset:49152
	ds_read_b128 v[164:167], v209 offset:32768
	ds_read_b128 v[168:171], v202 offset:49152
	ds_read_b128 v[172:175], v209 offset:34816
	v_mfma_f32_16x16x32_bf16 v[48:51], v[180:183], v[242:245], v[48:51]
	v_add_f32_e32 v221, v221, v85
	v_add_f32_e32 v220, v220, v82
	v_mfma_f32_16x16x32_bf16 v[52:55], v[180:183], v[204:207], v[52:55]
	v_add_f32_e32 v221, v221, v86
	ds_read_b128 v[176:179], v203 offset:49152
	v_mfma_f32_16x16x32_bf16 v[92:95], v[230:233], v[124:127], v[92:95]
	v_add_f32_e32 v220, v220, v83
	v_add_f32_e32 v221, v221, v87
	v_mfma_f32_16x16x32_bf16 v[88:91], v[230:233], v[108:111], v[88:91]
	v_cvt_pk_bf16_f32 v218, v72, v73
	ds_read_b128 v[180:183], v209 offset:36864
	v_mfma_f32_16x16x32_bf16 v[60:63], v[234:237], v[204:207], v[60:63]
	v_cvt_pk_bf16_f32 v219, v74, v75
	v_cvt_pk_bf16_f32 v240, v76, v77
	v_mfma_f32_16x16x32_bf16 v[56:59], v[234:237], v[242:245], v[56:59]
	v_cvt_pk_bf16_f32 v241, v78, v79
	ds_read_b128 v[230:233], v246 offset:49152
	s_waitcnt lgkmcnt(6)
	v_mfma_f32_16x16x32_bf16 v[64:67], v[160:163], v[96:99], 0
	v_exp_f32_e32 v88, v88
	v_mfma_f32_16x16x32_bf16 v[68:71], v[160:163], v[112:115], 0
	v_exp_f32_e32 v92, v92
	ds_read_b128 v[234:237], v209 offset:38912
	s_add_u32 s8, s16, 0x3bc00300
	s_addc_u32 s9, s17, 0
	s_add_u32 s6, s15, 0x23a70000
	s_addc_u32 s7, s14, 0
	s_waitcnt lgkmcnt(6)
	v_mfma_f32_16x16x32_bf16 v[0:3], v[164:167], v[216:219], v[0:3]
	v_cvt_pk_bf16_f32 v242, v80, v81
	v_mfma_f32_16x16x32_bf16 v[4:7], v[164:167], v[238:241], v[4:7]
	v_exp_f32_e32 v89, v89
	ds_read_b128 v[160:163], v201 offset:53248
	s_waitcnt vmcnt(4)
	ds_write_b128 v225, v[152:155] offset:16384
	s_waitcnt lgkmcnt(7)
	v_mfma_f32_16x16x32_bf16 v[68:71], v[168:171], v[116:119], v[68:71]
	v_exp_f32_e32 v93, v93
	v_mfma_f32_16x16x32_bf16 v[64:67], v[168:171], v[100:103], v[64:67]
	v_cvt_pk_bf16_f32 v243, v82, v83
	ds_read_b128 v[164:167], v209 offset:40960
	ds_write_b128 v226, v[156:159] offset:16384
	s_waitcnt lgkmcnt(8)
	v_mfma_f32_16x16x32_bf16 v[12:15], v[172:175], v[238:241], v[12:15]
	v_exp_f32_e32 v90, v90
	v_mfma_f32_16x16x32_bf16 v[8:11], v[172:175], v[216:219], v[8:11]
	v_exp_f32_e32 v94, v94
	ds_read_b128 v[168:171], v202 offset:53248
	ds_write_b64 v227, v[132:133] offset:0
	s_waitcnt lgkmcnt(9)
	v_mfma_f32_16x16x32_bf16 v[64:67], v[176:179], v[104:107], v[64:67]
	v_cvt_pk_bf16_f32 v204, v84, v85
	v_mfma_f32_16x16x32_bf16 v[68:71], v[176:179], v[120:123], v[68:71]
	v_exp_f32_e32 v91, v91
	ds_read_b128 v[172:175], v209 offset:43008
	ds_write_b64 v228, v[134:135] offset:0
	s_waitcnt lgkmcnt(10)
	v_mfma_f32_16x16x32_bf16 v[16:19], v[180:183], v[216:219], v[16:19]
	v_exp_f32_e32 v95, v95
	v_mfma_f32_16x16x32_bf16 v[20:23], v[180:183], v[238:241], v[20:23]
	v_cvt_pk_bf16_f32 v205, v86, v87
	v_add_f32_e32 v220, v220, v88
	ds_read_b128 v[176:179], v203 offset:53248
	ds_write_b64 v229, v[128:129] offset:0
	s_waitcnt lgkmcnt(11)
	v_mfma_f32_16x16x32_bf16 v[68:71], v[230:233], v[124:127], v[68:71]
	v_add_f32_e32 v221, v221, v92
	v_add_f32_e32 v220, v220, v89
	v_mfma_f32_16x16x32_bf16 v[64:67], v[230:233], v[108:111], v[64:67]
	v_add_f32_e32 v221, v221, v93
	v_cvt_pk_bf16_f32 v244, v88, v89
	ds_read_b128 v[180:183], v209 offset:45056
	ds_write_b64 v184, v[130:131] offset:0
	s_waitcnt lgkmcnt(12)
	v_mfma_f32_16x16x32_bf16 v[28:31], v[234:237], v[238:241], v[28:31]
	v_cvt_pk_bf16_f32 v245, v90, v91
	v_cvt_pk_bf16_f32 v206, v92, v93
	v_mfma_f32_16x16x32_bf16 v[24:27], v[234:237], v[216:219], v[24:27]
	v_cvt_pk_bf16_f32 v207, v94, v95
	ds_read_b128 v[230:233], v246 offset:53248
	global_load_dwordx4 v[132:135], v198, s[8:9]
	s_waitcnt lgkmcnt(12)
	v_mfma_f32_16x16x32_bf16 v[72:75], v[160:163], v[96:99], 0
	v_add_f32_e32 v220, v220, v90
	v_add_f32_e32 v221, v221, v94
	v_mfma_f32_16x16x32_bf16 v[76:79], v[160:163], v[112:115], 0
	v_add_f32_e32 v220, v220, v91
	v_add_f32_e32 v221, v221, v95
	ds_read_b128 v[234:237], v209 offset:47104
	global_load_dwordx4 v[128:131], v199, s[8:9]
	s_waitcnt lgkmcnt(11)
	v_mfma_f32_16x16x32_bf16 v[32:35], v[164:167], v[216:219], v[32:35]
	v_add_f32_e32 v194, v194, v220
	v_add_f32_e32 v195, v195, v221
	v_mfma_f32_16x16x32_bf16 v[36:39], v[164:167], v[238:241], v[36:39]
	v_exp_f32_e32 v64, v64
	ds_read_b128 v[160:163], v201 offset:57344
	global_load_dwordx4 v[152:155], v196, s[6:7]
	s_waitcnt lgkmcnt(10)
	v_mfma_f32_16x16x32_bf16 v[76:79], v[168:171], v[116:119], v[76:79]
	v_exp_f32_e32 v68, v68
	v_mfma_f32_16x16x32_bf16 v[72:75], v[168:171], v[100:103], v[72:75]
	v_exp_f32_e32 v65, v65
	ds_read_b128 v[164:167], v210 offset:32768
	global_load_dwordx4 v[156:159], v197, s[6:7]
	s_waitcnt lgkmcnt(9)
	v_mfma_f32_16x16x32_bf16 v[44:47], v[172:175], v[238:241], v[44:47]
	v_exp_f32_e32 v69, v69
	v_mfma_f32_16x16x32_bf16 v[40:43], v[172:175], v[216:219], v[40:43]
	v_exp_f32_e32 v66, v66
	ds_read_b128 v[168:171], v202 offset:57344
	s_waitcnt lgkmcnt(8)
	v_mfma_f32_16x16x32_bf16 v[72:75], v[176:179], v[104:107], v[72:75]
	v_exp_f32_e32 v70, v70
	v_mfma_f32_16x16x32_bf16 v[76:79], v[176:179], v[120:123], v[76:79]
	v_exp_f32_e32 v67, v67
	ds_read_b128 v[172:175], v210 offset:34816
	s_waitcnt lgkmcnt(7)
	v_mfma_f32_16x16x32_bf16 v[48:51], v[180:183], v[216:219], v[48:51]
	v_exp_f32_e32 v71, v71
	v_mfma_f32_16x16x32_bf16 v[52:55], v[180:183], v[238:241], v[52:55]
	v_add_f32_e32 v220, v64, v65
	ds_read_b128 v[176:179], v203 offset:57344
	s_waitcnt lgkmcnt(6)
	v_mfma_f32_16x16x32_bf16 v[76:79], v[230:233], v[124:127], v[76:79]
	v_add_f32_e32 v221, v68, v69
	v_mfma_f32_16x16x32_bf16 v[72:75], v[230:233], v[108:111], v[72:75]
	v_add_f32_e32 v220, v220, v66
	ds_read_b128 v[180:183], v210 offset:36864
	s_waitcnt lgkmcnt(6)
	v_mfma_f32_16x16x32_bf16 v[60:63], v[234:237], v[238:241], v[60:63]
	v_add_f32_e32 v221, v221, v70
	v_add_f32_e32 v220, v220, v67
	v_mfma_f32_16x16x32_bf16 v[56:59], v[234:237], v[216:219], v[56:59]
	v_add_f32_e32 v221, v221, v71
	ds_read_b128 v[230:233], v246 offset:57344
	s_waitcnt lgkmcnt(6)
	v_mfma_f32_16x16x32_bf16 v[80:83], v[160:163], v[96:99], 0
	v_exp_f32_e32 v72, v72
	v_mfma_f32_16x16x32_bf16 v[84:87], v[160:163], v[112:115], 0
	v_exp_f32_e32 v76, v76
	ds_read_b128 v[234:237], v210 offset:38912
	s_waitcnt lgkmcnt(6)
	v_mfma_f32_16x16x32_bf16 v[0:3], v[164:167], v[242:245], v[0:3]
	v_exp_f32_e32 v73, v73
	v_mfma_f32_16x16x32_bf16 v[4:7], v[164:167], v[204:207], v[4:7]
	v_exp_f32_e32 v77, v77
	ds_read_b128 v[160:163], v201 offset:61440
	s_waitcnt lgkmcnt(6)
	v_mfma_f32_16x16x32_bf16 v[84:87], v[168:171], v[116:119], v[84:87]
	v_exp_f32_e32 v74, v74
	v_mfma_f32_16x16x32_bf16 v[80:83], v[168:171], v[100:103], v[80:83]
	v_exp_f32_e32 v78, v78
	ds_read_b128 v[164:167], v210 offset:40960
	s_waitcnt lgkmcnt(6)
	v_mfma_f32_16x16x32_bf16 v[12:15], v[172:175], v[204:207], v[12:15]
	v_exp_f32_e32 v75, v75
	v_mfma_f32_16x16x32_bf16 v[8:11], v[172:175], v[242:245], v[8:11]
	v_exp_f32_e32 v79, v79
	ds_read_b128 v[168:171], v202 offset:61440
	s_waitcnt lgkmcnt(6)
	v_mfma_f32_16x16x32_bf16 v[80:83], v[176:179], v[104:107], v[80:83]
	v_add_f32_e32 v220, v220, v72
	v_add_f32_e32 v221, v221, v76
	v_mfma_f32_16x16x32_bf16 v[84:87], v[176:179], v[120:123], v[84:87]
	v_add_f32_e32 v220, v220, v73
	ds_read_b128 v[172:175], v210 offset:43008
	s_waitcnt lgkmcnt(6)
	v_mfma_f32_16x16x32_bf16 v[16:19], v[180:183], v[242:245], v[16:19]
	v_add_f32_e32 v221, v221, v77
	v_add_f32_e32 v220, v220, v74
	v_mfma_f32_16x16x32_bf16 v[20:23], v[180:183], v[204:207], v[20:23]
	v_add_f32_e32 v221, v221, v78
	ds_read_b128 v[176:179], v203 offset:61440
	s_waitcnt lgkmcnt(6)
	v_mfma_f32_16x16x32_bf16 v[84:87], v[230:233], v[124:127], v[84:87]
	v_add_f32_e32 v220, v220, v75
	v_add_f32_e32 v221, v221, v79
	v_mfma_f32_16x16x32_bf16 v[80:83], v[230:233], v[108:111], v[80:83]
	v_cvt_pk_bf16_f32 v216, v64, v65
	ds_read_b128 v[180:183], v210 offset:45056
	s_waitcnt lgkmcnt(6)
	v_mfma_f32_16x16x32_bf16 v[28:31], v[234:237], v[204:207], v[28:31]
	v_cvt_pk_bf16_f32 v217, v66, v67
	v_cvt_pk_bf16_f32 v238, v68, v69
	v_mfma_f32_16x16x32_bf16 v[24:27], v[234:237], v[242:245], v[24:27]
	v_cvt_pk_bf16_f32 v239, v70, v71
	ds_read_b128 v[230:233], v246 offset:61440
	s_waitcnt lgkmcnt(6)
	v_mfma_f32_16x16x32_bf16 v[88:91], v[160:163], v[96:99], 0
	v_exp_f32_e32 v80, v80
	v_mfma_f32_16x16x32_bf16 v[92:95], v[160:163], v[112:115], 0
	v_exp_f32_e32 v84, v84
	ds_read_b128 v[234:237], v210 offset:47104
	s_waitcnt lgkmcnt(6)
	v_mfma_f32_16x16x32_bf16 v[32:35], v[164:167], v[242:245], v[32:35]
	v_exp_f32_e32 v81, v81
	v_mfma_f32_16x16x32_bf16 v[36:39], v[164:167], v[204:207], v[36:39]
	v_exp_f32_e32 v85, v85
	ds_read_b128 v[160:163], v201 offset:0
	s_waitcnt lgkmcnt(6)
	v_mfma_f32_16x16x32_bf16 v[92:95], v[168:171], v[116:119], v[92:95]
	v_exp_f32_e32 v82, v82
	v_mfma_f32_16x16x32_bf16 v[88:91], v[168:171], v[100:103], v[88:91]
	v_exp_f32_e32 v86, v86
	ds_read_b128 v[164:167], v209 offset:49152
	s_waitcnt lgkmcnt(6)
	v_mfma_f32_16x16x32_bf16 v[44:47], v[172:175], v[204:207], v[44:47]
	v_exp_f32_e32 v83, v83
	v_mfma_f32_16x16x32_bf16 v[40:43], v[172:175], v[242:245], v[40:43]
	v_exp_f32_e32 v87, v87
	ds_read_b128 v[168:171], v202 offset:0
	s_waitcnt lgkmcnt(6)
	v_mfma_f32_16x16x32_bf16 v[88:91], v[176:179], v[104:107], v[88:91]
	v_add_f32_e32 v220, v220, v80
	v_add_f32_e32 v221, v221, v84
	v_mfma_f32_16x16x32_bf16 v[92:95], v[176:179], v[120:123], v[92:95]
	v_add_f32_e32 v220, v220, v81
	ds_read_b128 v[172:175], v209 offset:51200
	s_waitcnt lgkmcnt(6)
	v_mfma_f32_16x16x32_bf16 v[48:51], v[180:183], v[242:245], v[48:51]
	v_add_f32_e32 v221, v221, v85
	v_add_f32_e32 v220, v220, v82
	v_mfma_f32_16x16x32_bf16 v[52:55], v[180:183], v[204:207], v[52:55]
	v_add_f32_e32 v221, v221, v86
	ds_read_b128 v[176:179], v203 offset:0
	s_waitcnt lgkmcnt(6)
	v_mfma_f32_16x16x32_bf16 v[92:95], v[230:233], v[124:127], v[92:95]
	v_add_f32_e32 v220, v220, v83
	v_add_f32_e32 v221, v221, v87
	v_mfma_f32_16x16x32_bf16 v[88:91], v[230:233], v[108:111], v[88:91]
	v_cvt_pk_bf16_f32 v218, v72, v73
	ds_read_b128 v[180:183], v209 offset:53248
	s_waitcnt lgkmcnt(6)
	v_mfma_f32_16x16x32_bf16 v[60:63], v[234:237], v[204:207], v[60:63]
	v_cvt_pk_bf16_f32 v219, v74, v75
	v_cvt_pk_bf16_f32 v240, v76, v77
	v_mfma_f32_16x16x32_bf16 v[56:59], v[234:237], v[242:245], v[56:59]
	v_cvt_pk_bf16_f32 v241, v78, v79
	ds_read_b128 v[230:233], v246 offset:0
	s_waitcnt lgkmcnt(6)
	v_mfma_f32_16x16x32_bf16 v[64:67], v[160:163], v[96:99], 0
	v_exp_f32_e32 v88, v88
	v_mfma_f32_16x16x32_bf16 v[68:71], v[160:163], v[112:115], 0
	v_exp_f32_e32 v92, v92
	ds_read_b128 v[234:237], v209 offset:55296
	s_add_u32 s8, s16, 0x3bc00380
	s_addc_u32 s9, s17, 0
	s_add_u32 s6, s15, 0x23a80000
	s_addc_u32 s7, s14, 0
	s_waitcnt lgkmcnt(6)
	v_mfma_f32_16x16x32_bf16 v[0:3], v[164:167], v[216:219], v[0:3]
	v_cvt_pk_bf16_f32 v242, v80, v81
	v_mfma_f32_16x16x32_bf16 v[4:7], v[164:167], v[238:241], v[4:7]
	v_exp_f32_e32 v89, v89
	ds_read_b128 v[160:163], v201 offset:4096
	s_waitcnt vmcnt(4)
	ds_write_b128 v225, v[136:139] offset:32768
	s_waitcnt lgkmcnt(7)
	v_mfma_f32_16x16x32_bf16 v[68:71], v[168:171], v[116:119], v[68:71]
	v_exp_f32_e32 v93, v93
	v_mfma_f32_16x16x32_bf16 v[64:67], v[168:171], v[100:103], v[64:67]
	v_cvt_pk_bf16_f32 v243, v82, v83
	ds_read_b128 v[164:167], v209 offset:57344
	ds_write_b128 v226, v[140:143] offset:32768
	s_waitcnt lgkmcnt(8)
	v_mfma_f32_16x16x32_bf16 v[12:15], v[172:175], v[238:241], v[12:15]
	v_exp_f32_e32 v90, v90
	v_mfma_f32_16x16x32_bf16 v[8:11], v[172:175], v[216:219], v[8:11]
	v_exp_f32_e32 v94, v94
	ds_read_b128 v[168:171], v202 offset:4096
	ds_write_b64 v227, v[148:149] offset:16384
	s_waitcnt lgkmcnt(9)
	v_mfma_f32_16x16x32_bf16 v[64:67], v[176:179], v[104:107], v[64:67]
	v_cvt_pk_bf16_f32 v204, v84, v85
	v_mfma_f32_16x16x32_bf16 v[68:71], v[176:179], v[120:123], v[68:71]
	v_exp_f32_e32 v91, v91
	ds_read_b128 v[172:175], v209 offset:59392
	ds_write_b64 v228, v[150:151] offset:16384
	s_waitcnt lgkmcnt(10)
	v_mfma_f32_16x16x32_bf16 v[16:19], v[180:183], v[216:219], v[16:19]
	v_exp_f32_e32 v95, v95
	v_mfma_f32_16x16x32_bf16 v[20:23], v[180:183], v[238:241], v[20:23]
	v_cvt_pk_bf16_f32 v205, v86, v87
	v_add_f32_e32 v220, v220, v88
	ds_read_b128 v[176:179], v203 offset:4096
	ds_write_b64 v229, v[144:145] offset:16384
	s_waitcnt lgkmcnt(11)
	v_mfma_f32_16x16x32_bf16 v[68:71], v[230:233], v[124:127], v[68:71]
	v_add_f32_e32 v221, v221, v92
	v_add_f32_e32 v220, v220, v89
	v_mfma_f32_16x16x32_bf16 v[64:67], v[230:233], v[108:111], v[64:67]
	v_add_f32_e32 v221, v221, v93
	v_cvt_pk_bf16_f32 v244, v88, v89
	ds_read_b128 v[180:183], v209 offset:61440
	ds_write_b64 v184, v[146:147] offset:16384
	s_waitcnt lgkmcnt(12)
	v_mfma_f32_16x16x32_bf16 v[28:31], v[234:237], v[238:241], v[28:31]
	v_cvt_pk_bf16_f32 v245, v90, v91
	v_cvt_pk_bf16_f32 v206, v92, v93
	v_mfma_f32_16x16x32_bf16 v[24:27], v[234:237], v[216:219], v[24:27]
	v_cvt_pk_bf16_f32 v207, v94, v95
	ds_read_b128 v[230:233], v246 offset:4096
	global_load_dwordx4 v[148:151], v198, s[8:9]
	s_waitcnt lgkmcnt(12)
	v_mfma_f32_16x16x32_bf16 v[72:75], v[160:163], v[96:99], 0
	v_add_f32_e32 v220, v220, v90
	v_add_f32_e32 v221, v221, v94
	v_mfma_f32_16x16x32_bf16 v[76:79], v[160:163], v[112:115], 0
	v_add_f32_e32 v220, v220, v91
	v_add_f32_e32 v221, v221, v95
	ds_read_b128 v[234:237], v209 offset:63488
	global_load_dwordx4 v[144:147], v199, s[8:9]
	s_waitcnt lgkmcnt(11)
	v_mfma_f32_16x16x32_bf16 v[32:35], v[164:167], v[216:219], v[32:35]
	v_add_f32_e32 v194, v194, v220
	v_add_f32_e32 v195, v195, v221
	v_mfma_f32_16x16x32_bf16 v[36:39], v[164:167], v[238:241], v[36:39]
	v_exp_f32_e32 v64, v64
	ds_read_b128 v[160:163], v201 offset:8192
	global_load_dwordx4 v[136:139], v196, s[6:7]
	s_waitcnt lgkmcnt(10)
	v_mfma_f32_16x16x32_bf16 v[76:79], v[168:171], v[116:119], v[76:79]
	v_exp_f32_e32 v68, v68
	v_mfma_f32_16x16x32_bf16 v[72:75], v[168:171], v[100:103], v[72:75]
	v_exp_f32_e32 v65, v65
	ds_read_b128 v[164:167], v210 offset:49152
	global_load_dwordx4 v[140:143], v197, s[6:7]
	s_waitcnt lgkmcnt(9)
	v_mfma_f32_16x16x32_bf16 v[44:47], v[172:175], v[238:241], v[44:47]
	v_exp_f32_e32 v69, v69
	v_mfma_f32_16x16x32_bf16 v[40:43], v[172:175], v[216:219], v[40:43]
	v_exp_f32_e32 v66, v66
	ds_read_b128 v[168:171], v202 offset:8192
	s_waitcnt lgkmcnt(8)
	v_mfma_f32_16x16x32_bf16 v[72:75], v[176:179], v[104:107], v[72:75]
	v_exp_f32_e32 v70, v70
	v_mfma_f32_16x16x32_bf16 v[76:79], v[176:179], v[120:123], v[76:79]
	v_exp_f32_e32 v67, v67
	ds_read_b128 v[172:175], v210 offset:51200
	s_waitcnt lgkmcnt(7)
	v_mfma_f32_16x16x32_bf16 v[48:51], v[180:183], v[216:219], v[48:51]
	v_exp_f32_e32 v71, v71
	v_mfma_f32_16x16x32_bf16 v[52:55], v[180:183], v[238:241], v[52:55]
	v_add_f32_e32 v220, v64, v65
	ds_read_b128 v[176:179], v203 offset:8192
	s_waitcnt lgkmcnt(6)
	v_mfma_f32_16x16x32_bf16 v[76:79], v[230:233], v[124:127], v[76:79]
	v_add_f32_e32 v221, v68, v69
	v_mfma_f32_16x16x32_bf16 v[72:75], v[230:233], v[108:111], v[72:75]
	v_add_f32_e32 v220, v220, v66
	ds_read_b128 v[180:183], v210 offset:53248
	s_waitcnt lgkmcnt(6)
	v_mfma_f32_16x16x32_bf16 v[60:63], v[234:237], v[238:241], v[60:63]
	v_add_f32_e32 v221, v221, v70
	v_add_f32_e32 v220, v220, v67
	v_mfma_f32_16x16x32_bf16 v[56:59], v[234:237], v[216:219], v[56:59]
	v_add_f32_e32 v221, v221, v71
	ds_read_b128 v[230:233], v246 offset:8192
	s_waitcnt lgkmcnt(6)
	v_mfma_f32_16x16x32_bf16 v[80:83], v[160:163], v[96:99], 0
	v_exp_f32_e32 v72, v72
	v_mfma_f32_16x16x32_bf16 v[84:87], v[160:163], v[112:115], 0
	v_exp_f32_e32 v76, v76
	ds_read_b128 v[234:237], v210 offset:55296
	s_waitcnt lgkmcnt(6)
	v_mfma_f32_16x16x32_bf16 v[0:3], v[164:167], v[242:245], v[0:3]
	v_exp_f32_e32 v73, v73
	v_mfma_f32_16x16x32_bf16 v[4:7], v[164:167], v[204:207], v[4:7]
	v_exp_f32_e32 v77, v77
	ds_read_b128 v[160:163], v201 offset:12288
	s_waitcnt lgkmcnt(6)
	v_mfma_f32_16x16x32_bf16 v[84:87], v[168:171], v[116:119], v[84:87]
	v_exp_f32_e32 v74, v74
	v_mfma_f32_16x16x32_bf16 v[80:83], v[168:171], v[100:103], v[80:83]
	v_exp_f32_e32 v78, v78
	ds_read_b128 v[164:167], v210 offset:57344
	s_waitcnt lgkmcnt(6)
	v_mfma_f32_16x16x32_bf16 v[12:15], v[172:175], v[204:207], v[12:15]
	v_exp_f32_e32 v75, v75
	v_mfma_f32_16x16x32_bf16 v[8:11], v[172:175], v[242:245], v[8:11]
	v_exp_f32_e32 v79, v79
	ds_read_b128 v[168:171], v202 offset:12288
	s_waitcnt lgkmcnt(6)
	v_mfma_f32_16x16x32_bf16 v[80:83], v[176:179], v[104:107], v[80:83]
	v_add_f32_e32 v220, v220, v72
	v_add_f32_e32 v221, v221, v76
	v_mfma_f32_16x16x32_bf16 v[84:87], v[176:179], v[120:123], v[84:87]
	v_add_f32_e32 v220, v220, v73
	ds_read_b128 v[172:175], v210 offset:59392
	s_add_u32 s10, s10, 0x200
	s_addc_u32 s11, s11, 0
	s_add_u32 s12, s12, 0x40000
	s_addc_u32 s13, s13, 0
	s_add_i32 s4, s4, 4
	s_cmpk_lt_u32 s4, 0x104
	s_cselect_b64 s[6:7], -1, 0
	s_and_b64 s[6:7], s[0:1], s[6:7]
	s_and_b64 vcc, exec, s[6:7]
	s_waitcnt lgkmcnt(6)
	v_mfma_f32_16x16x32_bf16 v[16:19], v[180:183], v[242:245], v[16:19]
	v_add_f32_e32 v221, v221, v77
	v_add_f32_e32 v220, v220, v74
	v_mfma_f32_16x16x32_bf16 v[20:23], v[180:183], v[204:207], v[20:23]
	v_add_f32_e32 v221, v221, v78
	ds_read_b128 v[176:179], v203 offset:12288
	s_waitcnt lgkmcnt(6)
	v_mfma_f32_16x16x32_bf16 v[84:87], v[230:233], v[124:127], v[84:87]
	v_add_f32_e32 v220, v220, v75
	v_add_f32_e32 v221, v221, v79
	v_mfma_f32_16x16x32_bf16 v[80:83], v[230:233], v[108:111], v[80:83]
	v_cvt_pk_bf16_f32 v216, v64, v65
	ds_read_b128 v[180:183], v210 offset:61440
	s_waitcnt lgkmcnt(6)
	v_mfma_f32_16x16x32_bf16 v[28:31], v[234:237], v[204:207], v[28:31]
	v_cvt_pk_bf16_f32 v217, v66, v67
	v_cvt_pk_bf16_f32 v238, v68, v69
	v_mfma_f32_16x16x32_bf16 v[24:27], v[234:237], v[242:245], v[24:27]
	v_cvt_pk_bf16_f32 v239, v70, v71
	ds_read_b128 v[230:233], v246 offset:12288
	s_waitcnt lgkmcnt(6)
	v_mfma_f32_16x16x32_bf16 v[88:91], v[160:163], v[96:99], 0
	v_exp_f32_e32 v80, v80
	v_mfma_f32_16x16x32_bf16 v[92:95], v[160:163], v[112:115], 0
	v_exp_f32_e32 v84, v84
	ds_read_b128 v[234:237], v210 offset:63488
	s_waitcnt lgkmcnt(6)
	v_mfma_f32_16x16x32_bf16 v[32:35], v[164:167], v[242:245], v[32:35]
	v_exp_f32_e32 v81, v81
	v_mfma_f32_16x16x32_bf16 v[36:39], v[164:167], v[204:207], v[36:39]
	v_exp_f32_e32 v85, v85
	s_waitcnt lgkmcnt(5)
	v_mfma_f32_16x16x32_bf16 v[92:95], v[168:171], v[116:119], v[92:95]
	v_exp_f32_e32 v82, v82
	v_mfma_f32_16x16x32_bf16 v[88:91], v[168:171], v[100:103], v[88:91]
	v_exp_f32_e32 v86, v86
	s_waitcnt lgkmcnt(4)
	v_mfma_f32_16x16x32_bf16 v[44:47], v[172:175], v[204:207], v[44:47]
	v_exp_f32_e32 v83, v83
	v_mfma_f32_16x16x32_bf16 v[40:43], v[172:175], v[242:245], v[40:43]
	v_exp_f32_e32 v87, v87
	s_waitcnt lgkmcnt(3)
	v_mfma_f32_16x16x32_bf16 v[88:91], v[176:179], v[104:107], v[88:91]
	v_add_f32_e32 v220, v220, v80
	v_add_f32_e32 v221, v221, v84
	v_mfma_f32_16x16x32_bf16 v[92:95], v[176:179], v[120:123], v[92:95]
	v_add_f32_e32 v220, v220, v81
	s_waitcnt lgkmcnt(0)
	s_barrier
	ds_read_b128 v[160:163], v201 offset:16384
	ds_read_b128 v[164:167], v209 offset:0
	ds_read_b128 v[168:171], v202 offset:16384
	ds_read_b128 v[172:175], v209 offset:2048
	v_mfma_f32_16x16x32_bf16 v[48:51], v[180:183], v[242:245], v[48:51]
	v_add_f32_e32 v221, v221, v85
	v_add_f32_e32 v220, v220, v82
	v_mfma_f32_16x16x32_bf16 v[52:55], v[180:183], v[204:207], v[52:55]
	v_add_f32_e32 v221, v221, v86
	ds_read_b128 v[176:179], v203 offset:16384
	v_mfma_f32_16x16x32_bf16 v[92:95], v[230:233], v[124:127], v[92:95]
	v_add_f32_e32 v220, v220, v83
	v_add_f32_e32 v221, v221, v87
	v_mfma_f32_16x16x32_bf16 v[88:91], v[230:233], v[108:111], v[88:91]
	v_cvt_pk_bf16_f32 v218, v72, v73
	ds_read_b128 v[180:183], v209 offset:4096
	v_mfma_f32_16x16x32_bf16 v[60:63], v[234:237], v[204:207], v[60:63]
	v_cvt_pk_bf16_f32 v219, v74, v75
	v_cvt_pk_bf16_f32 v240, v76, v77
	v_mfma_f32_16x16x32_bf16 v[56:59], v[234:237], v[242:245], v[56:59]
	v_cvt_pk_bf16_f32 v241, v78, v79
	ds_read_b128 v[230:233], v246 offset:16384
	s_cbranch_vccnz .LBB0_734
	s_waitcnt vmcnt(0)
	s_nop 7
	s_nop 7
	ds_swizzle_b32 v64, v194 offset:swizzle(SWAP,16)
	s_waitcnt lgkmcnt(0)
	v_add_f32_e32 v194, v194, v64
	v_mov_b32_e32 v65, v194
	s_nop 1
	v_permlane32_swap_b32_e32 v194, v65
	v_add_f32_e32 v194, v194, v65
	s_nop 0
	v_rcp_f32_e32 v66, v194
	ds_swizzle_b32 v64, v195 offset:swizzle(SWAP,16)
	s_waitcnt lgkmcnt(0)
	v_add_f32_e32 v195, v195, v64
	v_mov_b32_e32 v65, v195
	s_nop 1
	v_permlane32_swap_b32_e32 v195, v65
	v_add_f32_e32 v195, v195, v65
	s_nop 0
	v_rcp_f32_e32 v67, v195
	v_readlane_b32 s100, v250, 8
	v_mbcnt_lo_u32_b32 v68, -1, 0
	v_mbcnt_hi_u32_b32 v68, -1, v68
	v_and_b32_e32 v69, 15, v68
	v_lshrrev_b32_e32 v70, 4, v68
	s_lshr_b32 s101, s100, 1
	v_add_u32_e32 v69, s101, v69
	v_lshlrev_b32_e32 v69, 12, v69
	v_and_b32_e32 v71, 1, v70
	v_lshlrev_b32_e32 v71, 5, v71
	v_and_b32_e32 v70, 2, v70
	v_lshl_add_u32 v71, v70, 3, v71
	v_add_u32_e32 v70, v69, v71
	v_add_u32_e32 v71, 0x10000, v70
	v_mul_f32_e32 v0, v0, v66
	v_mul_f32_e32 v1, v1, v66
	v_mul_f32_e32 v2, v2, v66
	v_mul_f32_e32 v3, v3, v66
	v_mul_f32_e32 v8, v8, v66
	v_mul_f32_e32 v9, v9, v66
	v_mul_f32_e32 v10, v10, v66
	v_mul_f32_e32 v11, v11, v66
	v_cvt_pk_bf16_f32 v72, v0, v1
	v_cvt_pk_bf16_f32 v73, v2, v3
	v_cvt_pk_bf16_f32 v74, v8, v9
	v_cvt_pk_bf16_f32 v75, v10, v11
	s_nop 1
	v_permlane16_swap_b32_e32 v72, v74
	v_permlane16_swap_b32_e32 v73, v75
	s_nop 1
	global_store_dwordx4 v70, v[72:75], s[58:59] offset:0
	v_mul_f32_e32 v16, v16, v66
	v_mul_f32_e32 v17, v17, v66
	v_mul_f32_e32 v18, v18, v66
	v_mul_f32_e32 v19, v19, v66
	v_mul_f32_e32 v24, v24, v66
	v_mul_f32_e32 v25, v25, v66
	v_mul_f32_e32 v26, v26, v66
	v_mul_f32_e32 v27, v27, v66
	v_cvt_pk_bf16_f32 v76, v16, v17
	v_cvt_pk_bf16_f32 v77, v18, v19
	v_cvt_pk_bf16_f32 v78, v24, v25
	v_cvt_pk_bf16_f32 v79, v26, v27
	s_nop 1
	v_permlane16_swap_b32_e32 v76, v78
	v_permlane16_swap_b32_e32 v77, v79
	s_nop 1
	global_store_dwordx4 v70, v[76:79], s[58:59] offset:64
	v_mul_f32_e32 v32, v32, v66
	v_mul_f32_e32 v33, v33, v66
	v_mul_f32_e32 v34, v34, v66
	v_mul_f32_e32 v35, v35, v66
	v_mul_f32_e32 v40, v40, v66
	v_mul_f32_e32 v41, v41, v66
	v_mul_f32_e32 v42, v42, v66
	v_mul_f32_e32 v43, v43, v66
	v_cvt_pk_bf16_f32 v80, v32, v33
	v_cvt_pk_bf16_f32 v81, v34, v35
	v_cvt_pk_bf16_f32 v82, v40, v41
	v_cvt_pk_bf16_f32 v83, v42, v43
	s_nop 1
	v_permlane16_swap_b32_e32 v80, v82
	v_permlane16_swap_b32_e32 v81, v83
	s_nop 1
	global_store_dwordx4 v70, v[80:83], s[58:59] offset:128
	v_mul_f32_e32 v48, v48, v66
	v_mul_f32_e32 v49, v49, v66
	v_mul_f32_e32 v50, v50, v66
	v_mul_f32_e32 v51, v51, v66
	v_mul_f32_e32 v56, v56, v66
	v_mul_f32_e32 v57, v57, v66
	v_mul_f32_e32 v58, v58, v66
	v_mul_f32_e32 v59, v59, v66
	v_cvt_pk_bf16_f32 v84, v48, v49
	v_cvt_pk_bf16_f32 v85, v50, v51
	v_cvt_pk_bf16_f32 v86, v56, v57
	v_cvt_pk_bf16_f32 v87, v58, v59
	s_nop 1
	v_permlane16_swap_b32_e32 v84, v86
	v_permlane16_swap_b32_e32 v85, v87
	s_nop 1
	global_store_dwordx4 v70, v[84:87], s[58:59] offset:192
	v_mul_f32_e32 v4, v4, v67
	v_mul_f32_e32 v5, v5, v67
	v_mul_f32_e32 v6, v6, v67
	v_mul_f32_e32 v7, v7, v67
	v_mul_f32_e32 v12, v12, v67
	v_mul_f32_e32 v13, v13, v67
	v_mul_f32_e32 v14, v14, v67
	v_mul_f32_e32 v15, v15, v67
	v_cvt_pk_bf16_f32 v88, v4, v5
	v_cvt_pk_bf16_f32 v89, v6, v7
	v_cvt_pk_bf16_f32 v90, v12, v13
	v_cvt_pk_bf16_f32 v91, v14, v15
	s_nop 1
	v_permlane16_swap_b32_e32 v88, v90
	v_permlane16_swap_b32_e32 v89, v91
	s_nop 1
	global_store_dwordx4 v71, v[88:91], s[58:59] offset:0
	v_mul_f32_e32 v20, v20, v67
	v_mul_f32_e32 v21, v21, v67
	v_mul_f32_e32 v22, v22, v67
	v_mul_f32_e32 v23, v23, v67
	v_mul_f32_e32 v28, v28, v67
	v_mul_f32_e32 v29, v29, v67
	v_mul_f32_e32 v30, v30, v67
	v_mul_f32_e32 v31, v31, v67
	v_cvt_pk_bf16_f32 v92, v20, v21
	v_cvt_pk_bf16_f32 v93, v22, v23
	v_cvt_pk_bf16_f32 v94, v28, v29
	v_cvt_pk_bf16_f32 v95, v30, v31
	s_nop 1
	v_permlane16_swap_b32_e32 v92, v94
	v_permlane16_swap_b32_e32 v93, v95
	s_nop 1
	global_store_dwordx4 v71, v[92:95], s[58:59] offset:64
	v_mul_f32_e32 v36, v36, v67
	v_mul_f32_e32 v37, v37, v67
	v_mul_f32_e32 v38, v38, v67
	v_mul_f32_e32 v39, v39, v67
	v_mul_f32_e32 v44, v44, v67
	v_mul_f32_e32 v45, v45, v67
	v_mul_f32_e32 v46, v46, v67
	v_mul_f32_e32 v47, v47, v67
	v_cvt_pk_bf16_f32 v72, v36, v37
	v_cvt_pk_bf16_f32 v73, v38, v39
	v_cvt_pk_bf16_f32 v74, v44, v45
	v_cvt_pk_bf16_f32 v75, v46, v47
	s_nop 1
	v_permlane16_swap_b32_e32 v72, v74
	v_permlane16_swap_b32_e32 v73, v75
	s_nop 1
	global_store_dwordx4 v71, v[72:75], s[58:59] offset:128
	v_mul_f32_e32 v52, v52, v67
	v_mul_f32_e32 v53, v53, v67
	v_mul_f32_e32 v54, v54, v67
	v_mul_f32_e32 v55, v55, v67
	v_mul_f32_e32 v60, v60, v67
	v_mul_f32_e32 v61, v61, v67
	v_mul_f32_e32 v62, v62, v67
	v_mul_f32_e32 v63, v63, v67
	v_cvt_pk_bf16_f32 v76, v52, v53
	v_cvt_pk_bf16_f32 v77, v54, v55
	v_cvt_pk_bf16_f32 v78, v60, v61
	v_cvt_pk_bf16_f32 v79, v62, v63
	s_nop 1
	v_permlane16_swap_b32_e32 v76, v78
	v_permlane16_swap_b32_e32 v77, v79
	s_nop 1
	global_store_dwordx4 v71, v[76:79], s[58:59] offset:192
	s_barrier
